# speedup vs baseline: 1.0118x; 1.0063x over previous
.LBB1_27:
	s_or_b64 exec, exec, s[0:1]
	v_mul_lo_u16_e32 v2, 0x56, v66
	v_mov_b32_e32 v3, 3
	v_mul_lo_u16_sdwa v2, v2, v3 dst_sel:DWORD dst_unused:UNUSED_PAD src0_sel:BYTE_1 src1_sel:DWORD
	v_sub_u16_e32 v2, v66, v2
	v_mov_b32_e32 v4, 0
	v_cmp_eq_u16_sdwa s[0:1], v2, v4 src0_sel:BYTE_0 src1_sel:DWORD
	v_and_b32_e32 v168, 31, v0
	v_lshrrev_b32_e32 v174, 5, v67
	v_cndmask_b32_e64 v19, 32, 0, s[0:1]
	v_or_b32_e32 v4, v19, v168
	v_cndmask_b32_e64 v5, v165, v166, s[4:5]
	v_mul_u32_u24_e32 v4, 0x190, v4
	v_lshlrev_b32_e32 v169, 4, v174
	v_add3_u32 v32, v5, v4, v169
	v_mov_b32_e32 v3, 2
	ds_read_b128 v[20:23], v32
	v_cmp_eq_u16_sdwa s[0:1], v2, v3 src0_sel:BYTE_0 src1_sel:DWORD
	v_lshlrev_b32_e32 v171, 2, v174
	v_or_b32_e32 v19, v19, v171
	v_cndmask_b32_e64 v2, 0, 32, s[0:1]
	v_or_b32_e32 v18, v2, v168
	v_mul_u32_u24_e32 v2, 0x190, v18
	v_add3_u32 v33, v166, v2, v169
	ds_read_b128 v[24:27], v33
	v_add_u32_e32 v170, 0x1bc00, v173
	v_add_u32_e32 v175, 0x20000, v173
	s_movk_i32 s3, 0x110
	v_lshlrev_b32_e32 v226, 2, v19
	v_lshlrev_b32_e32 v227, 2, v18
	v_add_u32_e32 v228, v164, v226
	v_add_u32_e32 v229, v164, v227
	v_mov_b32_e32 v230, 0x100
	v_cndmask_b32_e64 v230, 0, v230, s[4:5]
	v_add3_u32 v230, v167, v230, v226
	v_add_u32_e32 v231, v167, v227
	ds_read_b32 v224, v229
	ds_read_b32 v225, v231 offset:256
	ds_read_b128 v[176:179], v228 offset:0
	ds_read_b128 v[180:183], v228 offset:32
	ds_read_b128 v[184:187], v228 offset:64
	ds_read_b128 v[188:191], v228 offset:96
	ds_read_b128 v[192:195], v230 offset:0
	ds_read_b128 v[196:199], v230 offset:32
	ds_read_b128 v[200:203], v230 offset:64
	ds_read_b128 v[204:207], v230 offset:96
	ds_read_b128 v[28:31], v32 offset:32
	ds_read_b128 v[120:123], v33 offset:32
	v_readfirstlane_b32 s44, v66
	s_waitcnt lgkmcnt(12)
	v_mfma_f32_32x32x2_f32 v[2:17], v20, v24, 0
	v_mfma_f32_32x32x2_f32 v[2:17], v21, v25, v[2:17]
	v_mfma_f32_32x32x2_f32 v[2:17], v22, v26, v[2:17]
	v_mfma_f32_32x32x2_f32 v[2:17], v23, v27, v[2:17]
	ds_read_b128 v[20:23], v32 offset:64
	ds_read_b128 v[24:27], v33 offset:64
	s_waitcnt lgkmcnt(2)
	v_mfma_f32_32x32x2_f32 v[2:17], v28, v120, v[2:17]
	v_sub_f32_e32 v176, v176, v224
	v_min_f32_e32 v176, 0, v176
	v_mul_f32_e32 v176, 0x3fb8aa3b, v176
	v_exp_f32_e32 v176, v176
	v_mov_b32_e32 v226, v19
	v_mul_f32_e32 v176, v192, v176
	v_cmp_le_u32_e32 vcc, v18, v226
	v_mul_f32_e32 v176, v225, v176
	v_mfma_f32_32x32x2_f32 v[2:17], v29, v121, v[2:17]
	s_nop 0
	v_cndmask_b32_e32 v176, 0, v176, vcc
	v_sub_f32_e32 v177, v177, v224
	v_min_f32_e32 v177, 0, v177
	v_mul_f32_e32 v177, 0x3fb8aa3b, v177
	v_exp_f32_e32 v177, v177
	v_or_b32_e32 v226, 1, v19
	v_mul_f32_e32 v177, v193, v177
	v_mfma_f32_32x32x2_f32 v[2:17], v30, v122, v[2:17]
	v_cmp_le_u32_e32 vcc, v18, v226
	v_mul_f32_e32 v177, v225, v177
	s_nop 0
	v_cndmask_b32_e32 v177, 0, v177, vcc
	v_sub_f32_e32 v178, v178, v224
	v_min_f32_e32 v178, 0, v178
	v_mul_f32_e32 v178, 0x3fb8aa3b, v178
	v_exp_f32_e32 v178, v178
	v_mfma_f32_32x32x2_f32 v[2:17], v31, v123, v[2:17]
	v_or_b32_e32 v226, 2, v19
	v_mul_f32_e32 v178, v194, v178
	v_cmp_le_u32_e32 vcc, v18, v226
	v_mul_f32_e32 v178, v225, v178
	s_nop 0
	v_cndmask_b32_e32 v178, 0, v178, vcc
	v_sub_f32_e32 v179, v179, v224
	v_min_f32_e32 v179, 0, v179
	ds_read_b128 v[28:31], v32 offset:96
	ds_read_b128 v[120:123], v33 offset:96
	s_waitcnt lgkmcnt(2)
	v_mfma_f32_32x32x2_f32 v[2:17], v20, v24, v[2:17]
	v_mul_f32_e32 v179, 0x3fb8aa3b, v179
	v_exp_f32_e32 v179, v179
	v_or_b32_e32 v226, 3, v19
	v_mul_f32_e32 v179, v195, v179
	v_cmp_le_u32_e32 vcc, v18, v226
	v_mul_f32_e32 v179, v225, v179
	s_nop 0
	v_cndmask_b32_e32 v179, 0, v179, vcc
	v_mfma_f32_32x32x2_f32 v[2:17], v21, v25, v[2:17]
	v_sub_f32_e32 v180, v180, v224
	v_min_f32_e32 v180, 0, v180
	v_mul_f32_e32 v180, 0x3fb8aa3b, v180
	v_exp_f32_e32 v180, v180
	v_or_b32_e32 v226, 8, v19
	v_mul_f32_e32 v180, v196, v180
	v_cmp_le_u32_e32 vcc, v18, v226
	v_mul_f32_e32 v180, v225, v180
	v_mfma_f32_32x32x2_f32 v[2:17], v22, v26, v[2:17]
	s_nop 0
	v_cndmask_b32_e32 v180, 0, v180, vcc
	v_sub_f32_e32 v181, v181, v224
	v_min_f32_e32 v181, 0, v181
	v_mul_f32_e32 v181, 0x3fb8aa3b, v181
	v_exp_f32_e32 v181, v181
	v_or_b32_e32 v226, 9, v19
	v_mul_f32_e32 v181, v197, v181
	v_mfma_f32_32x32x2_f32 v[2:17], v23, v27, v[2:17]
	v_cmp_le_u32_e32 vcc, v18, v226
	v_mul_f32_e32 v181, v225, v181
	s_nop 0
	v_cndmask_b32_e32 v181, 0, v181, vcc
	v_sub_f32_e32 v182, v182, v224
	v_min_f32_e32 v182, 0, v182
	v_mul_f32_e32 v182, 0x3fb8aa3b, v182
	v_exp_f32_e32 v182, v182
	ds_read_b128 v[20:23], v32 offset:128
	ds_read_b128 v[24:27], v33 offset:128
	s_waitcnt lgkmcnt(2)
	v_mfma_f32_32x32x2_f32 v[2:17], v28, v120, v[2:17]
	v_or_b32_e32 v226, 10, v19
	v_mul_f32_e32 v182, v198, v182
	v_cmp_le_u32_e32 vcc, v18, v226
	v_mul_f32_e32 v182, v225, v182
	s_nop 0
	v_cndmask_b32_e32 v182, 0, v182, vcc
	v_sub_f32_e32 v183, v183, v224
	v_min_f32_e32 v183, 0, v183
	v_mfma_f32_32x32x2_f32 v[2:17], v29, v121, v[2:17]
	v_mul_f32_e32 v183, 0x3fb8aa3b, v183
	v_exp_f32_e32 v183, v183
	v_or_b32_e32 v226, 11, v19
	v_mul_f32_e32 v183, v199, v183
	v_cmp_le_u32_e32 vcc, v18, v226
	v_mul_f32_e32 v183, v225, v183
	s_nop 0
	v_cndmask_b32_e32 v183, 0, v183, vcc
	v_mfma_f32_32x32x2_f32 v[2:17], v30, v122, v[2:17]
	v_sub_f32_e32 v184, v184, v224
	v_min_f32_e32 v184, 0, v184
	v_mul_f32_e32 v184, 0x3fb8aa3b, v184
	v_exp_f32_e32 v184, v184
	v_or_b32_e32 v226, 16, v19
	v_mul_f32_e32 v184, v200, v184
	v_cmp_le_u32_e32 vcc, v18, v226
	v_mul_f32_e32 v184, v225, v184
	v_mfma_f32_32x32x2_f32 v[2:17], v31, v123, v[2:17]
	s_nop 0
	v_cndmask_b32_e32 v184, 0, v184, vcc
	v_sub_f32_e32 v185, v185, v224
	v_min_f32_e32 v185, 0, v185
	v_mul_f32_e32 v185, 0x3fb8aa3b, v185
	v_exp_f32_e32 v185, v185
	v_or_b32_e32 v226, 17, v19
	v_mul_f32_e32 v185, v201, v185
	ds_read_b128 v[28:31], v32 offset:160
	ds_read_b128 v[120:123], v33 offset:160
	s_waitcnt lgkmcnt(2)
	v_mfma_f32_32x32x2_f32 v[2:17], v20, v24, v[2:17]
	v_cmp_le_u32_e32 vcc, v18, v226
	v_mul_f32_e32 v185, v225, v185
	s_nop 0
	v_cndmask_b32_e32 v185, 0, v185, vcc
	v_sub_f32_e32 v186, v186, v224
	v_min_f32_e32 v186, 0, v186
	v_mul_f32_e32 v186, 0x3fb8aa3b, v186
	v_exp_f32_e32 v186, v186
	v_mfma_f32_32x32x2_f32 v[2:17], v21, v25, v[2:17]
	v_or_b32_e32 v226, 18, v19
	v_mul_f32_e32 v186, v202, v186
	v_cmp_le_u32_e32 vcc, v18, v226
	v_mul_f32_e32 v186, v225, v186
	s_nop 0
	v_cndmask_b32_e32 v186, 0, v186, vcc
	v_sub_f32_e32 v187, v187, v224
	v_min_f32_e32 v187, 0, v187
	v_mfma_f32_32x32x2_f32 v[2:17], v22, v26, v[2:17]
	v_mul_f32_e32 v187, 0x3fb8aa3b, v187
	v_exp_f32_e32 v187, v187
	v_or_b32_e32 v226, 19, v19
	v_mul_f32_e32 v187, v203, v187
	v_cmp_le_u32_e32 vcc, v18, v226
	v_mul_f32_e32 v187, v225, v187
	s_nop 0
	v_cndmask_b32_e32 v187, 0, v187, vcc
	v_mfma_f32_32x32x2_f32 v[2:17], v23, v27, v[2:17]
	v_sub_f32_e32 v188, v188, v224
	v_min_f32_e32 v188, 0, v188
	v_mul_f32_e32 v188, 0x3fb8aa3b, v188
	v_exp_f32_e32 v188, v188
	v_or_b32_e32 v226, 24, v19
	v_mul_f32_e32 v188, v204, v188
	v_cmp_le_u32_e32 vcc, v18, v226
	v_mul_f32_e32 v188, v225, v188
	ds_read_b128 v[20:23], v32 offset:192
	ds_read_b128 v[24:27], v33 offset:192
	s_waitcnt lgkmcnt(2)
	v_mfma_f32_32x32x2_f32 v[2:17], v28, v120, v[2:17]
	s_nop 0
	v_cndmask_b32_e32 v188, 0, v188, vcc
	v_sub_f32_e32 v189, v189, v224
	v_min_f32_e32 v189, 0, v189
	v_mul_f32_e32 v189, 0x3fb8aa3b, v189
	v_exp_f32_e32 v189, v189
	v_or_b32_e32 v226, 25, v19
	v_mul_f32_e32 v189, v205, v189
	v_mfma_f32_32x32x2_f32 v[2:17], v29, v121, v[2:17]
	v_cmp_le_u32_e32 vcc, v18, v226
	v_mul_f32_e32 v189, v225, v189
	s_nop 0
	v_cndmask_b32_e32 v189, 0, v189, vcc
	v_sub_f32_e32 v190, v190, v224
	v_min_f32_e32 v190, 0, v190
	v_mul_f32_e32 v190, 0x3fb8aa3b, v190
	v_exp_f32_e32 v190, v190
	v_mfma_f32_32x32x2_f32 v[2:17], v30, v122, v[2:17]
	v_or_b32_e32 v226, 26, v19
	v_mul_f32_e32 v190, v206, v190
	v_cmp_le_u32_e32 vcc, v18, v226
	v_mul_f32_e32 v190, v225, v190
	s_nop 0
	v_cndmask_b32_e32 v190, 0, v190, vcc
	v_sub_f32_e32 v191, v191, v224
	v_min_f32_e32 v191, 0, v191
	v_mfma_f32_32x32x2_f32 v[2:17], v31, v123, v[2:17]
	v_mul_f32_e32 v191, 0x3fb8aa3b, v191
	v_exp_f32_e32 v191, v191
	v_or_b32_e32 v226, 27, v19
	v_mul_f32_e32 v191, v207, v191
	v_cmp_le_u32_e32 vcc, v18, v226
	v_mul_f32_e32 v191, v225, v191
	s_nop 0
	v_cndmask_b32_e32 v191, 0, v191, vcc
	ds_read_b128 v[28:31], v32 offset:224
	ds_read_b128 v[120:123], v33 offset:224
	s_cmp_ge_u32 s44, 4
	s_cbranch_scc1 .Lp2_half_done
	s_waitcnt lgkmcnt(2)
	v_mfma_f32_32x32x2_f32 v[2:17], v20, v24, v[2:17]
	v_mfma_f32_32x32x2_f32 v[2:17], v21, v25, v[2:17]
	v_mfma_f32_32x32x2_f32 v[2:17], v22, v26, v[2:17]
	v_mfma_f32_32x32x2_f32 v[2:17], v23, v27, v[2:17]
	ds_read_b128 v[20:23], v32 offset:256
	ds_read_b128 v[24:27], v33 offset:256
	s_waitcnt lgkmcnt(2)
	v_mfma_f32_32x32x2_f32 v[2:17], v28, v120, v[2:17]
	v_mfma_f32_32x32x2_f32 v[2:17], v29, v121, v[2:17]
	v_mfma_f32_32x32x2_f32 v[2:17], v30, v122, v[2:17]
	v_mfma_f32_32x32x2_f32 v[2:17], v31, v123, v[2:17]
	ds_read_b128 v[28:31], v32 offset:288
	ds_read_b128 v[120:123], v33 offset:288
	s_waitcnt lgkmcnt(2)
	v_mfma_f32_32x32x2_f32 v[2:17], v20, v24, v[2:17]
	v_mfma_f32_32x32x2_f32 v[2:17], v21, v25, v[2:17]
	v_mfma_f32_32x32x2_f32 v[2:17], v22, v26, v[2:17]
	v_mfma_f32_32x32x2_f32 v[2:17], v23, v27, v[2:17]
	ds_read_b128 v[20:23], v32 offset:320
	ds_read_b128 v[24:27], v33 offset:320
	s_waitcnt lgkmcnt(2)
	v_mfma_f32_32x32x2_f32 v[2:17], v28, v120, v[2:17]
	v_mfma_f32_32x32x2_f32 v[2:17], v29, v121, v[2:17]
	v_mfma_f32_32x32x2_f32 v[2:17], v30, v122, v[2:17]
	v_mfma_f32_32x32x2_f32 v[2:17], v31, v123, v[2:17]
	ds_read_b128 v[28:31], v32 offset:352
	ds_read_b128 v[120:123], v33 offset:352
	s_waitcnt lgkmcnt(2)
	v_mfma_f32_32x32x2_f32 v[2:17], v20, v24, v[2:17]
	v_mfma_f32_32x32x2_f32 v[2:17], v21, v25, v[2:17]
	v_mfma_f32_32x32x2_f32 v[2:17], v22, v26, v[2:17]
	v_mfma_f32_32x32x2_f32 v[2:17], v23, v27, v[2:17]
	s_waitcnt lgkmcnt(0)
	v_mfma_f32_32x32x2_f32 v[2:17], v28, v120, v[2:17]
	v_mfma_f32_32x32x2_f32 v[2:17], v29, v121, v[2:17]
	v_mfma_f32_32x32x2_f32 v[2:17], v30, v122, v[2:17]
	v_mfma_f32_32x32x2_f32 v[2:17], v31, v123, v[2:17]
	s_cmp_lt_u32 s44, 2
	s_cbranch_scc1 .Lp2_half_done
	v_or_b32_e32 v254, 32, v168
	v_mul_u32_u24_e32 v254, 0x190, v254
	v_add3_u32 v252, v165, v254, v169
	v_add_u32_e32 v255, -2, v66
	v_lshlrev_b32_e32 v255, 5, v255
	v_or_b32_e32 v255, v255, v168
	v_mul_u32_u24_e32 v255, 0x190, v255
	v_add3_u32 v253, v166, v255, v169
	ds_read_b128 v[20:23], v252 offset:192
	ds_read_b128 v[24:27], v253 offset:192
	ds_read_b128 v[28:31], v252 offset:224
	ds_read_b128 v[120:123], v253 offset:224
	s_waitcnt lgkmcnt(2)
	v_mfma_f32_32x32x2_f32 v[236:251], v20, v24, 0
	v_mfma_f32_32x32x2_f32 v[236:251], v21, v25, v[236:251]
	v_mfma_f32_32x32x2_f32 v[236:251], v22, v26, v[236:251]
	v_mfma_f32_32x32x2_f32 v[236:251], v23, v27, v[236:251]
	ds_read_b128 v[20:23], v252 offset:256
	ds_read_b128 v[24:27], v253 offset:256
	s_waitcnt lgkmcnt(2)
	v_mfma_f32_32x32x2_f32 v[236:251], v28, v120, v[236:251]
	v_mfma_f32_32x32x2_f32 v[236:251], v29, v121, v[236:251]
	v_mfma_f32_32x32x2_f32 v[236:251], v30, v122, v[236:251]
	v_mfma_f32_32x32x2_f32 v[236:251], v31, v123, v[236:251]
	ds_read_b128 v[28:31], v252 offset:288
	ds_read_b128 v[120:123], v253 offset:288
	s_waitcnt lgkmcnt(2)
	v_mfma_f32_32x32x2_f32 v[236:251], v20, v24, v[236:251]
	v_mfma_f32_32x32x2_f32 v[236:251], v21, v25, v[236:251]
	v_mfma_f32_32x32x2_f32 v[236:251], v22, v26, v[236:251]
	v_mfma_f32_32x32x2_f32 v[236:251], v23, v27, v[236:251]
	ds_read_b128 v[20:23], v252 offset:320
	ds_read_b128 v[24:27], v253 offset:320
	s_waitcnt lgkmcnt(2)
	v_mfma_f32_32x32x2_f32 v[236:251], v28, v120, v[236:251]
	v_mfma_f32_32x32x2_f32 v[236:251], v29, v121, v[236:251]
	v_mfma_f32_32x32x2_f32 v[236:251], v30, v122, v[236:251]
	v_mfma_f32_32x32x2_f32 v[236:251], v31, v123, v[236:251]
	ds_read_b128 v[28:31], v252 offset:352
	ds_read_b128 v[120:123], v253 offset:352
	s_waitcnt lgkmcnt(2)
	v_mfma_f32_32x32x2_f32 v[236:251], v20, v24, v[236:251]
	v_mfma_f32_32x32x2_f32 v[236:251], v21, v25, v[236:251]
	v_mfma_f32_32x32x2_f32 v[236:251], v22, v26, v[236:251]
	v_mfma_f32_32x32x2_f32 v[236:251], v23, v27, v[236:251]
	s_waitcnt lgkmcnt(0)
	v_mfma_f32_32x32x2_f32 v[236:251], v28, v120, v[236:251]
	v_mfma_f32_32x32x2_f32 v[236:251], v29, v121, v[236:251]
	v_mfma_f32_32x32x2_f32 v[236:251], v30, v122, v[236:251]
	v_mfma_f32_32x32x2_f32 v[236:251], v31, v123, v[236:251]
	v_lshlrev_b32_e32 v254, 2, v67
	v_add_u32_e32 v255, -2, v66
	v_lshl_add_u32 v254, v255, 12, v254
	v_add_u32_e32 v254, 0x15800, v254
	s_nop 15
	s_nop 3
	ds_write_b32 v254, v236
	ds_write_b32 v254, v237 offset:256
	ds_write_b32 v254, v238 offset:512
	ds_write_b32 v254, v239 offset:768
	ds_write_b32 v254, v240 offset:1024
	ds_write_b32 v254, v241 offset:1280
	ds_write_b32 v254, v242 offset:1536
	ds_write_b32 v254, v243 offset:1792
	ds_write_b32 v254, v244 offset:2048
	ds_write_b32 v254, v245 offset:2304
	ds_write_b32 v254, v246 offset:2560
	ds_write_b32 v254, v247 offset:2816
	ds_write_b32 v254, v248 offset:3072
	ds_write_b32 v254, v249 offset:3328
	ds_write_b32 v254, v250 offset:3584
	ds_write_b32 v254, v251 offset:3840
.Lp2_half_done:
	s_waitcnt lgkmcnt(0)
	s_barrier
	s_cmp_lt_u32 s44, 4
	s_cbranch_scc1 .Lp2_noadd
	v_lshlrev_b32_e32 v254, 2, v67
	v_add_u32_e32 v255, -4, v66
	v_lshl_add_u32 v254, v255, 12, v254
	v_add_u32_e32 v254, 0x15800, v254
	ds_read_b32 v236, v254
	ds_read_b32 v237, v254 offset:256
	ds_read_b32 v238, v254 offset:512
	ds_read_b32 v239, v254 offset:768
	ds_read_b32 v240, v254 offset:1024
	ds_read_b32 v241, v254 offset:1280
	ds_read_b32 v242, v254 offset:1536
	ds_read_b32 v243, v254 offset:1792
	ds_read_b32 v244, v254 offset:2048
	ds_read_b32 v245, v254 offset:2304
	ds_read_b32 v246, v254 offset:2560
	ds_read_b32 v247, v254 offset:2816
	ds_read_b32 v248, v254 offset:3072
	ds_read_b32 v249, v254 offset:3328
	ds_read_b32 v250, v254 offset:3584
	ds_read_b32 v251, v254 offset:3840
	s_waitcnt lgkmcnt(0)
	v_add_f32_e32 v2, v2, v236
	v_add_f32_e32 v3, v3, v237
	v_add_f32_e32 v4, v4, v238
	v_add_f32_e32 v5, v5, v239
	v_add_f32_e32 v6, v6, v240
	v_add_f32_e32 v7, v7, v241
	v_add_f32_e32 v8, v8, v242
	v_add_f32_e32 v9, v9, v243
	v_add_f32_e32 v10, v10, v244
	v_add_f32_e32 v11, v11, v245
	v_add_f32_e32 v12, v12, v246
	v_add_f32_e32 v13, v13, v247
	v_add_f32_e32 v14, v14, v248
	v_add_f32_e32 v15, v15, v249
	v_add_f32_e32 v16, v16, v250
	v_add_f32_e32 v17, v17, v251
.Lp2_noadd:
	s_and_b64 vcc, exec, s[6:7]
	s_cbranch_vccz .Lp2_amt
	v_mad_u32_u24 v227, v19, s3, v227
	v_add_u32_e32 v227, v170, v227
	v_mul_f32_e32 v176, 0x3dd105ec, v176
	v_mul_f32_e32 v177, 0x3dd105ec, v177
	v_mul_f32_e32 v178, 0x3dd105ec, v178
	v_mul_f32_e32 v179, 0x3dd105ec, v179
	v_mul_f32_e32 v180, 0x3dd105ec, v180
	v_mul_f32_e32 v181, 0x3dd105ec, v181
	v_mul_f32_e32 v182, 0x3dd105ec, v182
	v_mul_f32_e32 v183, 0x3dd105ec, v183
	v_mul_f32_e32 v184, 0x3dd105ec, v184
	v_mul_f32_e32 v185, 0x3dd105ec, v185
	v_mul_f32_e32 v186, 0x3dd105ec, v186
	v_mul_f32_e32 v187, 0x3dd105ec, v187
	v_mul_f32_e32 v188, 0x3dd105ec, v188
	v_mul_f32_e32 v189, 0x3dd105ec, v189
	v_mul_f32_e32 v190, 0x3dd105ec, v190
	v_mul_f32_e32 v191, 0x3dd105ec, v191
	s_nop 7
	v_mul_f32_e32 v176, v2, v176
	v_mul_f32_e32 v177, v3, v177
	v_mul_f32_e32 v178, v4, v178
	v_mul_f32_e32 v179, v5, v179
	v_mul_f32_e32 v180, v6, v180
	v_mul_f32_e32 v181, v7, v181
	v_mul_f32_e32 v182, v8, v182
	v_mul_f32_e32 v183, v9, v183
	v_mul_f32_e32 v184, v10, v184
	v_mul_f32_e32 v185, v11, v185
	v_mul_f32_e32 v186, v12, v186
	v_mul_f32_e32 v187, v13, v187
	v_mul_f32_e32 v188, v14, v188
	v_mul_f32_e32 v189, v15, v189
	v_mul_f32_e32 v190, v16, v190
	v_mul_f32_e32 v191, v17, v191
	ds_write_b32 v227, v176
	ds_write_b32 v227, v177 offset:272
	ds_write_b32 v227, v178 offset:544
	ds_write_b32 v227, v179 offset:816
	ds_write_b32 v227, v180 offset:2176
	ds_write_b32 v227, v181 offset:2448
	ds_write_b32 v227, v182 offset:2720
	ds_write_b32 v227, v183 offset:2992
	ds_write_b32 v227, v184 offset:4352
	ds_write_b32 v227, v185 offset:4624
	ds_write_b32 v227, v186 offset:4896
	ds_write_b32 v227, v187 offset:5168
	ds_write_b32 v227, v188 offset:6528
	ds_write_b32 v227, v189 offset:6800
	ds_write_b32 v227, v190 offset:7072
	ds_write_b32 v227, v191 offset:7344
	s_branch .Lp2_done
